# speedup vs baseline: 1.0488x; 1.0171x over previous
_Z5cvt_wPKfPDF16_S0_S1_iPi:
	s_cmp_lg_u32 s2, 0
	s_cbranch_scc1 .Lcw_exit
	s_load_dwordx2 s[4:5], s[0:1], 0x28
	s_load_dwordx2 s[6:7], s[0:1], 0x0
	v_lshlrev_b32_e32 v1, 2, v0
	v_mov_b32_e32 v2, 0
	s_waitcnt lgkmcnt(0)
	global_store_dword v1, v2, s[4:5]
	v_mov_b32_e32 v4, s6
	v_mov_b32_e32 v5, s7
	v_cmp_eq_u32_e32 vcc, 0, v0
	s_and_saveexec_b64 s[8:9], vcc
	global_store_dwordx2 v1, v[4:5], s[4:5] offset:1024

_Z8moe_gemmILi1024ELi2048ELb1EEvPKDF16_S1_PKfPDF16_PfPKiS7_:
	v_lshl_or_b32 v216, s2, 8, v0
	v_and_b32_e32 v217, 63, v216
	v_lshrrev_b32_e32 v216, 6, v216
	v_lshlrev_b32_e32 v215, 3, v217
	v_lshlrev_b32_e32 v214, 4, v217
	v_lshl_add_u32 v217, v216, 10, v215
	v_lshl_add_u32 v216, v216, 11, v214
	s_mov_b32 s96, 16
	s_mov_b32 s97, 0
	s_mov_b32 s98, 0
	s_load_dwordx2 s[4:5], s[0:1], 0x28
	v_readfirstlane_b32 s12, v0
	s_waitcnt lgkmcnt(0)
	s_load_dwordx2 s[92:93], s[4:5], 0x400
	s_add_u32 s94, s4, 0x6000000
	s_addc_u32 s95, s5, 0
	s_load_dword s23, s[4:5], 0x0
	s_load_dword s25, s[4:5], 0x80
	s_load_dword s27, s[4:5], 0x100
	s_load_dword s29, s[4:5], 0x180
	s_load_dword s31, s[4:5], 0x200
	s_load_dword s33, s[4:5], 0x280
	s_load_dword s35, s[4:5], 0x300
	s_load_dword s38, s[4:5], 0x380
	s_waitcnt lgkmcnt(0)
	s_add_i32 s3, s23, 0x9f
	s_mul_hi_i32 s3, s3, 0x66666667
	s_lshr_b32 s4, s3, 31
	s_ashr_i32 s39, s3, 6
	s_add_i32 s3, s25, 0x9f
	s_mul_hi_i32 s3, s3, 0x66666667
	s_add_i32 s39, s39, s4
	s_lshr_b32 s4, s3, 31
	s_ashr_i32 s40, s3, 6
	s_add_i32 s40, s40, s4
	s_add_i32 s4, s27, 0x9f
	s_mul_hi_i32 s4, s4, 0x66666667
	s_lshr_b32 s5, s4, 31
	s_ashr_i32 s41, s4, 6
	s_add_i32 s4, s29, 0x9f
	s_mul_hi_i32 s4, s4, 0x66666667
	s_add_i32 s41, s41, s5
	s_lshr_b32 s5, s4, 31
	s_ashr_i32 s42, s4, 6
	s_add_i32 s4, s31, 0x9f
	s_mul_hi_i32 s4, s4, 0x66666667
	s_add_i32 s42, s42, s5
	s_lshr_b32 s5, s4, 31
	s_ashr_i32 s43, s4, 6
	s_add_i32 s4, s33, 0x9f
	s_mul_hi_i32 s4, s4, 0x66666667
	s_add_i32 s3, s40, s39
	s_add_i32 s43, s43, s5
	s_lshr_b32 s5, s4, 31
	s_ashr_i32 s44, s4, 6
	s_add_i32 s4, s35, 0x9f
	s_add_i32 s3, s41, s3
	s_mul_hi_i32 s4, s4, 0x66666667
	s_add_i32 s3, s42, s3
	s_add_i32 s44, s44, s5
	s_lshr_b32 s5, s4, 31
	s_ashr_i32 s45, s4, 6
	s_add_i32 s4, s38, 0x9f
	s_add_i32 s3, s43, s3
	s_mul_hi_i32 s4, s4, 0x66666667
	s_add_i32 s3, s44, s3
	s_add_i32 s45, s45, s5
	s_lshr_b32 s5, s4, 31
	s_ashr_i32 s46, s4, 6
	s_add_i32 s3, s45, s3
	s_add_i32 s46, s46, s5
	s_add_i32 s3, s46, s3
	s_lshl_b32 s3, s3, 4
	s_and_b32 s4, s2, 7
	s_mul_i32 s4, s3, s4
	s_lshr_b32 s2, s2, 3
	s_ashr_i32 s5, s4, 3
	s_add_i32 s4, s4, s3
	s_ashr_i32 s47, s4, 3
	s_add_i32 s48, s5, s2
	s_cmp_ge_i32 s48, s47
	s_cbranch_scc1 .LBB2_78
	s_load_dword s13, s[0:1], 0x38
	s_load_dwordx2 s[2:3], s[0:1], 0x30
	s_load_dwordx8 s[4:11], s[0:1], 0x0
	v_bfe_u32 v1, v0, 4, 2
	v_lshrrev_b32_e32 v2, 5, v0
	s_waitcnt lgkmcnt(0)
	s_lshr_b32 s49, s13, 3
	s_bfe_u32 s1, s12, 0x10006
	v_and_or_b32 v2, v2, 4, v1
	v_lshrrev_b32_e32 v5, 7, v0
	s_cmpk_lt_u32 s12, 0x80
	v_lshlrev_b32_e32 v2, 4, v2
	v_lshlrev_b32_e32 v3, 3, v0
	s_movk_i32 s0, 0x78
	v_bfe_u32 v4, v0, 4, 3
	v_bitop3_b32 v5, v5, v0, 7 bitop3:0x78
	v_lshlrev_b32_e32 v6, 6, v0
	s_cselect_b64 s[12:13], -1, 0
	v_bitop3_b32 v2, v2, v3, s0 bitop3:0x78
	v_xor_b32_e32 v5, v5, v4
	s_lshl_b32 s0, s1, 6
	v_lshlrev_b32_e32 v4, 2, v1
	v_lshlrev_b32_e32 v1, 11, v1
	v_and_b32_e32 v6, 0x300, v6
	v_and_b32_e32 v8, 8, v3
	v_lshrrev_b32_e32 v101, 4, v0
	v_and_b32_e32 v103, 15, v0
	v_lshrrev_b32_e32 v124, 3, v0
	v_lshl_add_u32 v125, v0, 4, 0
	v_or3_b32 v1, v1, v6, v8
	v_bfe_u32 v6, v0, 1, 3
	v_or_b32_e32 v0, s0, v4
	v_and_b32_e32 v7, 0xe0, v3
	v_lshl_add_u32 v100, v0, 1, 0
	s_lshl_b32 s1, s1, 7
	v_and_b32_e32 v0, 16, v3
	v_or_b32_e32 v3, s1, v0
	v_bitop3_b32 v0, s1, v7, v0 bitop3:0x36
	v_or_b32_e32 v127, v0, v1
	v_bitop3_b32 v0, v3, v7, 32 bitop3:0x36
	v_or_b32_e32 v128, v0, v1
	v_bitop3_b32 v0, v3, v7, 64 bitop3:0x36
	s_movk_i32 s1, 0x60
	v_or_b32_e32 v129, v0, v1
	v_bitop3_b32 v0, v3, v7, s1 bitop3:0x36
	s_add_i32 s1, s23, 15
	s_lshr_b32 s1, s1, 4
	v_or_b32_e32 v130, v0, v1
	s_add_i32 s1, s39, s1
	v_cvt_f32_i32_e32 v0, s39
	s_add_i32 s1, s1, -1
	v_cvt_f32_i32_e32 v1, s1
	s_add_i32 s14, s25, 15
	v_rcp_iflag_f32_e32 v144, v0
	s_lshr_b32 s14, s14, 4
	v_add_f32_e32 v0, 0.5, v1
	v_cvt_f32_i32_e32 v1, s40
	s_add_i32 s14, s40, s14
	s_add_i32 s14, s14, -1
	v_mul_f32_e32 v0, v144, v0
	v_cvt_i32_f32_e32 v0, v0
	v_cvt_f32_i32_e32 v7, s14
	v_rcp_iflag_f32_e32 v145, v1
	s_add_i32 s16, s27, 15
	s_lshr_b32 s16, s16, 4
	v_cvt_f32_i32_e32 v1, s41
	s_add_i32 s16, s41, s16
	v_readfirstlane_b32 s1, v0
	v_add_f32_e32 v0, 0.5, v7
	s_add_i32 s16, s16, -1
	s_add_i32 s17, s29, 15
	s_add_i32 s18, s31, 15
	s_add_i32 s19, s33, 15
	s_add_i32 s20, s35, 15
	s_add_i32 s21, s38, 15
	v_mul_f32_e32 v0, v145, v0
	s_lshr_b32 s17, s17, 4
	s_lshr_b32 s18, s18, 4
	s_lshr_b32 s19, s19, 4
	s_lshr_b32 s20, s20, 4
	s_lshr_b32 s21, s21, 4
	v_cvt_i32_f32_e32 v0, v0
	v_cvt_f32_i32_e32 v7, s16
	s_add_i32 s17, s42, s17
	s_add_i32 s18, s43, s18
	s_add_i32 s19, s44, s19
	s_add_i32 s20, s45, s20
	s_add_i32 s21, s46, s21
	v_rcp_iflag_f32_e32 v146, v1
	s_add_i32 s50, 0, 0xe000
	s_lshl_b32 s52, s39, 4
	s_lshl_b32 s53, s40, 4
	s_lshl_b32 s54, s41, 4
	s_add_i32 s17, s17, -1
	s_lshl_b32 s55, s42, 4
	s_add_i32 s18, s18, -1
	s_lshl_b32 s56, s43, 4
	s_add_i32 s19, s19, -1
	s_lshl_b32 s57, s44, 4
	s_add_i32 s20, s20, -1
	s_lshl_b32 s58, s45, 4
	s_add_i32 s21, s21, -1
	s_lshl_b32 s59, s46, 4
	s_cmp_gt_i32 s23, 0
	v_cvt_f32_i32_e32 v1, s42
	s_cselect_b32 s60, s1, 0
	v_readfirstlane_b32 s1, v0
	v_add_f32_e32 v0, 0.5, v7
	v_mul_f32_e32 v0, v146, v0
	v_cvt_i32_f32_e32 v0, v0
	v_cvt_f32_i32_e32 v7, s17
	v_rcp_iflag_f32_e32 v147, v1
	s_cmp_gt_i32 s25, 0
	v_cvt_f32_i32_e32 v1, s43
	s_cselect_b32 s61, s1, 0
	v_readfirstlane_b32 s1, v0
	v_add_f32_e32 v0, 0.5, v7
	v_mul_f32_e32 v0, v147, v0
	v_cvt_i32_f32_e32 v0, v0
	v_cvt_f32_i32_e32 v7, s18
	v_rcp_iflag_f32_e32 v148, v1
	s_cmp_gt_i32 s27, 0
	v_cvt_f32_i32_e32 v1, s44
	s_cselect_b32 s62, s1, 0
	v_readfirstlane_b32 s1, v0
	v_add_f32_e32 v0, 0.5, v7
	v_mul_f32_e32 v0, v148, v0
	v_cvt_i32_f32_e32 v0, v0
	v_cvt_f32_i32_e32 v7, s19
	v_rcp_iflag_f32_e32 v149, v1
	s_cmp_gt_i32 s29, 0
	v_cvt_f32_i32_e32 v1, s45
	s_cselect_b32 s63, s1, 0
	v_readfirstlane_b32 s1, v0
	v_add_f32_e32 v0, 0.5, v7
	v_mul_f32_e32 v0, v149, v0
	v_cvt_i32_f32_e32 v0, v0
	v_cvt_f32_i32_e32 v7, s20
	v_rcp_iflag_f32_e32 v150, v1
	s_cmp_gt_i32 s31, 0
	s_cselect_b32 s64, s1, 0
	v_readfirstlane_b32 s1, v0
	v_add_f32_e32 v0, 0.5, v7
	v_mul_f32_e32 v0, v150, v0
	v_cvt_i32_f32_e32 v0, v0
	v_cvt_f32_i32_e32 v1, s46
	s_cmp_gt_i32 s33, 0
	s_cselect_b32 s65, s1, 0
	v_readfirstlane_b32 s1, v0
	v_cvt_f32_i32_e32 v0, s21
	v_rcp_iflag_f32_e32 v151, v1
	v_mov_b32_e32 v97, 0
	v_lshlrev_b32_e32 v96, 12, v101
	v_add_f32_e32 v0, 0.5, v0
	v_mul_f32_e32 v0, v151, v0
	v_cvt_i32_f32_e32 v7, v0
	v_lshlrev_b32_e32 v0, 4, v5
	v_mov_b32_e32 v1, v97
	v_lshl_add_u64 v[98:99], s[6:7], 0, v[96:97]
	s_cmp_gt_i32 s35, 0
	v_lshl_add_u64 v[104:105], s[4:5], 0, v[0:1]
	s_mov_b64 s[4:5], 0x80
	v_lshl_or_b32 v96, v2, 1, v96
	v_lshl_add_u32 v8, v103, 4, 0
	v_mul_u32_u24_e32 v3, 0x110, v101
	s_cselect_b32 s66, s1, 0
	s_cmp_gt_i32 s38, 0
	v_readfirstlane_b32 s1, v7
	v_lshl_add_u64 v[106:107], v[104:105], 0, s[4:5]
	v_lshl_add_u64 v[0:1], s[6:7], 0, v[96:97]
	s_mov_b64 s[4:5], 0x40000
	s_mov_b32 s15, 0
	v_lshlrev_b32_e32 v126, 7, v103
	v_lshlrev_b32_e32 v102, 3, v103
	v_add_u32_e32 v131, s50, v127
	v_add_u32_e32 v132, s50, v128
	v_add_u32_e32 v133, s50, v129
	v_add_u32_e32 v134, s50, v130
	s_movk_i32 s51, 0x110
	v_or_b32_e32 v135, 16, v101
	v_or_b32_e32 v136, 32, v101
	v_or_b32_e32 v137, 48, v101
	v_or_b32_e32 v138, 64, v101
	v_or_b32_e32 v139, 0x50, v101
	v_or_b32_e32 v140, 0x60, v101
	v_or_b32_e32 v141, 0x70, v101
	v_or_b32_e32 v142, 0x80, v101
	v_or_b32_e32 v143, 0x90, v101
	v_bitop3_b32 v152, v6, v101, 3 bitop3:0x78
	s_mul_i32 s67, s52, s60
	s_mul_i32 s68, s53, s61
	s_mul_i32 s69, s54, s62
	s_mul_i32 s70, s55, s63
	s_mul_i32 s71, s56, s64
	s_mul_i32 s72, s57, s65
	s_mul_i32 s73, s58, s66
	s_cselect_b32 s74, s1, 0
	v_lshl_add_u64 v[108:109], v[0:1], 0, s[4:5]
	s_lshl_b32 s6, s0, 2
	v_lshlrev_b32_e32 v153, 2, v4
	v_lshlrev_b32_e32 v96, 1, v2
	s_mov_b64 s[16:17], 0x10000
	s_mov_b64 s[18:19], 0x20000
	s_mov_b64 s[20:21], 0x30000
	s_mov_b32 s22, 0x3f3504f3
	s_mov_b32 s75, 0x3ea7ba05
	s_mov_b32 s24, 0xbfba00e3
	s_mov_b32 s26, 0x3f87dc22
	s_mov_b32 s28, 0x3fb5f0e3
	s_brev_b32 s76, -2
	v_add_u32_e32 v154, v8, v3
	s_movk_i32 s77, 0x1080
	s_mov_b32 s30, 0xbe91a98e
	s_mov_b32 s34, 0x3e827906
	s_add_i32 s99, s48, s49
	s_cmp_lt_i32 s99, s47
	s_cselect_b32 s98, 1, 0
	s_branch .LBB2_3

.LBB2_45:
	s_add_i32 s14, 0, 0x5000
	s_bitcmp1_b32 s80, 0
	s_cselect_b32 s14, s14, s50
	v_add_u32_e32 v200, s14, v127
	v_add_u32_e32 v201, s14, v128
	v_add_u32_e32 v202, s14, v129
	v_add_u32_e32 v203, s14, v130
	s_cselect_b32 s14, 0x9000, 0
	v_add_u32_e32 v204, s14, v125
	s_cselect_b32 s81, 0, 0x9000
	v_add_u32_e32 v198, 0x5000, v204
	v_add_u32_e32 v161, s81, v156
	v_readfirstlane_b32 s14, v198
	v_add_u32_e32 v205, 0x6000, v204
	v_add_u32_e32 v178, v161, v159
	v_add_u32_e32 v174, v161, v160
	s_mov_b32 m0, s14
	v_readfirstlane_b32 s14, v205
	v_add_u32_e32 v205, 0x7000, v204
	s_cmp_eq_u32 s97, 0
	s_cbranch_scc1 .Lw2k_w0
	s_waitcnt vmcnt(2) lgkmcnt(0)
	s_branch .Lw2k_w1
.Lw2k_w0:
	s_waitcnt vmcnt(0) lgkmcnt(0)
.Lw2k_w1:
	s_barrier
	ds_read_b128 v[162:165], v178
	ds_read_b128 v[166:169], v178 offset:4096
	ds_read_b128 v[170:173], v174 offset:6144
	ds_read_b128 v[174:177], v174 offset:2048
	ds_read_b128 v[178:181], v178 offset:8192
	ds_read_b64_tr_b16 v[182:183], v200 offset:0
	ds_read_b64_tr_b16 v[184:185], v200 offset:0x400
	ds_read_b64_tr_b16 v[186:187], v201 offset:0
	ds_read_b64_tr_b16 v[188:189], v201 offset:0x400
	ds_read_b64_tr_b16 v[190:191], v202 offset:0
	ds_read_b64_tr_b16 v[192:193], v202 offset:0x400
	ds_read_b64_tr_b16 v[194:195], v203 offset:0
	ds_read_b64_tr_b16 v[196:197], v203 offset:0x400
	global_load_lds_dwordx4 v[120:121], off sc1
	v_lshl_add_u64 v[198:199], v[120:121], 0, s[16:17]
	s_mov_b32 m0, s14
	v_readfirstlane_b32 s14, v205
	v_add_u32_e32 v205, 0x8000, v204
	global_load_lds_dwordx4 v[198:199], off sc1
	v_lshl_add_u64 v[198:199], v[120:121], 0, s[18:19]
	s_mov_b32 m0, s14
	v_readfirstlane_b32 s14, v205
	global_load_lds_dwordx4 v[198:199], off sc1
	v_lshl_add_u64 v[198:199], v[120:121], 0, s[20:21]
	s_mov_b32 m0, s14
	s_nop 0
	global_load_lds_dwordx4 v[198:199], off sc1
	s_waitcnt lgkmcnt(0)
	s_setprio 1
	s_waitcnt lgkmcnt(0)
	v_mfma_f32_16x16x32_f16 v[92:95], v[182:185], v[162:165], v[92:95]
	v_mfma_f32_16x16x32_f16 v[88:91], v[186:189], v[162:165], v[88:91]
	v_mfma_f32_16x16x32_f16 v[84:87], v[190:193], v[162:165], v[84:87]
	v_mfma_f32_16x16x32_f16 v[80:83], v[194:197], v[162:165], v[80:83]
	v_mfma_f32_16x16x32_f16 v[76:79], v[182:185], v[174:177], v[76:79]
	v_mfma_f32_16x16x32_f16 v[72:75], v[186:189], v[174:177], v[72:75]
	v_mfma_f32_16x16x32_f16 v[68:71], v[190:193], v[174:177], v[68:71]
	v_mfma_f32_16x16x32_f16 v[64:67], v[194:197], v[174:177], v[64:67]
	v_mfma_f32_16x16x32_f16 v[60:63], v[182:185], v[166:169], v[60:63]
	v_mfma_f32_16x16x32_f16 v[56:59], v[186:189], v[166:169], v[56:59]
	v_mfma_f32_16x16x32_f16 v[52:55], v[190:193], v[166:169], v[52:55]
	v_mfma_f32_16x16x32_f16 v[48:51], v[194:197], v[166:169], v[48:51]
	v_mfma_f32_16x16x32_f16 v[44:47], v[182:185], v[170:173], v[44:47]
	v_mfma_f32_16x16x32_f16 v[40:43], v[186:189], v[170:173], v[40:43]
	v_mfma_f32_16x16x32_f16 v[36:39], v[190:193], v[170:173], v[36:39]
	v_mfma_f32_16x16x32_f16 v[32:35], v[194:197], v[170:173], v[32:35]
	v_mfma_f32_16x16x32_f16 v[28:31], v[182:185], v[178:181], v[28:31]
	v_mfma_f32_16x16x32_f16 v[24:27], v[186:189], v[178:181], v[24:27]
	v_mfma_f32_16x16x32_f16 v[20:23], v[190:193], v[178:181], v[20:23]
	v_mfma_f32_16x16x32_f16 v[16:19], v[194:197], v[178:181], v[16:19]
	s_setprio 0
	v_add_u32_e32 v178, v161, v158
	v_add_u32_e32 v161, v161, v157
	ds_read_b128 v[162:165], v178
	ds_read_b128 v[166:169], v178 offset:4096
	ds_read_b128 v[170:173], v161 offset:6144
	ds_read_b128 v[174:177], v161 offset:2048
	ds_read_b128 v[178:181], v178 offset:8192
	v_readfirstlane_b32 s14, v204
	v_add_u32_e32 v161, 0x1000, v204
	v_lshl_add_u64 v[198:199], v[112:113], 0, s[0:1]
	s_mov_b32 m0, s14
	v_readfirstlane_b32 s14, v161
	v_add_u32_e32 v161, 0x2000, v204
	ds_read_b64_tr_b16 v[182:183], v200 offset:0x2000
	ds_read_b64_tr_b16 v[184:185], v200 offset:0x2400
	ds_read_b64_tr_b16 v[186:187], v201 offset:0x2000
	ds_read_b64_tr_b16 v[188:189], v201 offset:0x2400
	ds_read_b64_tr_b16 v[190:191], v202 offset:0x2000
	ds_read_b64_tr_b16 v[192:193], v202 offset:0x2400
	ds_read_b64_tr_b16 v[194:195], v203 offset:0x2000
	ds_read_b64_tr_b16 v[196:197], v203 offset:0x2400
	global_load_lds_dwordx4 v[198:199], off sc1
	v_lshl_add_u64 v[198:199], v[114:115], 0, s[0:1]
	s_mov_b32 m0, s14
	v_readfirstlane_b32 s14, v161
	v_add_u32_e32 v161, 0x3000, v204
	global_load_lds_dwordx4 v[198:199], off sc1
	v_lshl_add_u64 v[198:199], v[116:117], 0, s[0:1]
	s_mov_b32 m0, s14
	v_readfirstlane_b32 s14, v161
	v_add_u32_e32 v161, 0x4000, v204
	global_load_lds_dwordx4 v[198:199], off sc1
	v_lshl_add_u64 v[198:199], v[118:119], 0, s[0:1]
	s_mov_b32 m0, s14
	v_readfirstlane_b32 s14, v161
	global_load_lds_dwordx4 v[198:199], off sc1
	v_lshl_add_u64 v[198:199], v[122:123], 0, s[0:1]
	s_mov_b32 m0, s14
	s_nop 0
	global_load_lds_dwordx4 v[198:199], off sc1
	s_waitcnt lgkmcnt(0)
	s_setprio 1
	s_waitcnt lgkmcnt(0)
	v_mfma_f32_16x16x32_f16 v[92:95], v[182:185], v[162:165], v[92:95]
	v_mfma_f32_16x16x32_f16 v[88:91], v[186:189], v[162:165], v[88:91]
	v_mfma_f32_16x16x32_f16 v[84:87], v[190:193], v[162:165], v[84:87]
	v_mfma_f32_16x16x32_f16 v[80:83], v[194:197], v[162:165], v[80:83]
	v_mfma_f32_16x16x32_f16 v[76:79], v[182:185], v[174:177], v[76:79]
	v_mfma_f32_16x16x32_f16 v[72:75], v[186:189], v[174:177], v[72:75]
	v_mfma_f32_16x16x32_f16 v[68:71], v[190:193], v[174:177], v[68:71]
	v_mfma_f32_16x16x32_f16 v[64:67], v[194:197], v[174:177], v[64:67]
	v_mfma_f32_16x16x32_f16 v[60:63], v[182:185], v[166:169], v[60:63]
	v_mfma_f32_16x16x32_f16 v[56:59], v[186:189], v[166:169], v[56:59]
	v_mfma_f32_16x16x32_f16 v[52:55], v[190:193], v[166:169], v[52:55]
	v_mfma_f32_16x16x32_f16 v[48:51], v[194:197], v[166:169], v[48:51]
	v_mfma_f32_16x16x32_f16 v[44:47], v[182:185], v[170:173], v[44:47]
	v_mfma_f32_16x16x32_f16 v[40:43], v[186:189], v[170:173], v[40:43]
	v_mfma_f32_16x16x32_f16 v[36:39], v[190:193], v[170:173], v[36:39]
	v_mfma_f32_16x16x32_f16 v[32:35], v[194:197], v[170:173], v[32:35]
	v_mfma_f32_16x16x32_f16 v[28:31], v[182:185], v[178:181], v[28:31]
	v_mfma_f32_16x16x32_f16 v[24:27], v[186:189], v[178:181], v[24:27]
	v_mfma_f32_16x16x32_f16 v[20:23], v[190:193], v[178:181], v[20:23]
	v_mfma_f32_16x16x32_f16 v[16:19], v[194:197], v[178:181], v[16:19]
	s_setprio 0
	s_cmp_eq_u32 s97, 0
	s_cbranch_scc1 .Lw2k_noc
	s_waitcnt vmcnt(9)
	v_cvt_pk_f16_f32 v208, v208, v209
	v_cvt_pk_f16_f32 v209, v210, v211
	v_cvt_pk_f16_f32 v210, v212, v213
	v_cvt_pk_f16_f32 v211, v214, v215
	global_store_dwordx2 v217, v[208:209], s[94:95]
	global_store_dwordx2 v217, v[210:211], s[94:95] offset:512
	s_add_u32 s94, s94, 0x200000
	s_addc_u32 s95, s95, 0
	s_mov_b32 s97, 0
.Lw2k_noc:
	s_cmp_eq_u32 s96, 0
	s_cbranch_scc1 .Lw2k_nol
	s_and_b32 s99, s80, s98
	s_cmp_lg_u32 s99, 0
	s_cbranch_scc1 .Lw2k_nol
	global_load_dwordx4 v[208:211], v216, s[92:93] nt
	global_load_dwordx4 v[212:215], v216, s[92:93] offset:1024 nt
	s_add_u32 s92, s92, 0x400000
	s_addc_u32 s93, s93, 0
	s_sub_u32 s96, s96, 1
	s_mov_b32 s97, 1
.Lw2k_nol:
	s_add_u32 s0, s0, 0x80
	s_addc_u32 s1, s1, 0
	s_add_i32 s80, s80, 1
	s_cmpk_lg_i32 s0, 0x780
	v_lshl_add_u64 v[120:121], v[120:121], 0, s[4:5]
	s_cbranch_scc1 .LBB2_45
	v_add_u32_e32 v159, v156, v159
	v_add_u32_e32 v160, v156, v160
	s_waitcnt vmcnt(0)
	s_waitcnt vmcnt(0)
	s_barrier
	s_cmp_eq_u32 s97, 0
	s_cbranch_scc1 .Lw2k_p0
	v_cvt_pk_f16_f32 v208, v208, v209
	v_cvt_pk_f16_f32 v209, v210, v211
	v_cvt_pk_f16_f32 v210, v212, v213
	v_cvt_pk_f16_f32 v211, v214, v215
	global_store_dwordx2 v217, v[208:209], s[94:95]
	global_store_dwordx2 v217, v[210:211], s[94:95] offset:512
	s_add_u32 s94, s94, 0x200000
	s_addc_u32 s95, s95, 0
	s_mov_b32 s97, 0
.Lw2k_p0:
	ds_read_b128 v[112:115], v159 offset:36864
	ds_read_b128 v[116:119], v159 offset:40960
	ds_read_b128 v[120:123], v160 offset:43008
	ds_read_b128 v[160:163], v160 offset:38912
	ds_read_b128 v[164:167], v159 offset:45056
	ds_read_b64_tr_b16 v[168:169], v131 offset:0
	ds_read_b64_tr_b16 v[170:171], v131 offset:0x400
	ds_read_b64_tr_b16 v[172:173], v132 offset:0
	ds_read_b64_tr_b16 v[174:175], v132 offset:0x400
	ds_read_b64_tr_b16 v[176:177], v133 offset:0
	ds_read_b64_tr_b16 v[178:179], v133 offset:0x400
	ds_read_b64_tr_b16 v[180:181], v134 offset:0
	ds_read_b64_tr_b16 v[182:183], v134 offset:0x400
	s_waitcnt lgkmcnt(0)
	s_setprio 1
	s_waitcnt lgkmcnt(4)
	v_mfma_f32_16x16x32_f16 v[92:95], v[168:171], v[112:115], v[92:95]
	v_mfma_f32_16x16x32_f16 v[88:91], v[172:175], v[112:115], v[88:91]
	v_mfma_f32_16x16x32_f16 v[84:87], v[176:179], v[112:115], v[84:87]
	v_mfma_f32_16x16x32_f16 v[80:83], v[180:183], v[112:115], v[80:83]
	s_waitcnt lgkmcnt(1)
	v_mfma_f32_16x16x32_f16 v[76:79], v[168:171], v[160:163], v[76:79]
	v_mfma_f32_16x16x32_f16 v[72:75], v[172:175], v[160:163], v[72:75]
	v_mfma_f32_16x16x32_f16 v[68:71], v[176:179], v[160:163], v[68:71]
	v_mfma_f32_16x16x32_f16 v[64:67], v[180:183], v[160:163], v[64:67]
	v_mfma_f32_16x16x32_f16 v[60:63], v[168:171], v[116:119], v[60:63]
	v_mfma_f32_16x16x32_f16 v[56:59], v[172:175], v[116:119], v[56:59]
	v_mfma_f32_16x16x32_f16 v[52:55], v[176:179], v[116:119], v[52:55]
	v_mfma_f32_16x16x32_f16 v[48:51], v[180:183], v[116:119], v[48:51]
	v_mfma_f32_16x16x32_f16 v[44:47], v[168:171], v[120:123], v[44:47]
	v_mfma_f32_16x16x32_f16 v[40:43], v[172:175], v[120:123], v[40:43]
	v_mfma_f32_16x16x32_f16 v[36:39], v[176:179], v[120:123], v[36:39]
	v_mfma_f32_16x16x32_f16 v[32:35], v[180:183], v[120:123], v[32:35]
	s_waitcnt lgkmcnt(0)
	v_mfma_f32_16x16x32_f16 v[28:31], v[168:171], v[164:167], v[28:31]
	v_mfma_f32_16x16x32_f16 v[24:27], v[172:175], v[164:167], v[24:27]
	v_mfma_f32_16x16x32_f16 v[20:23], v[176:179], v[164:167], v[20:23]
	v_mfma_f32_16x16x32_f16 v[16:19], v[180:183], v[164:167], v[16:19]
	s_setprio 0
	v_add_u32_e32 v160, v156, v158
	v_add_u32_e32 v156, v156, v157
	ds_read_b128 v[112:115], v160 offset:36864
	ds_read_b128 v[116:119], v160 offset:40960
	ds_read_b128 v[120:123], v156 offset:43008
	ds_read_b128 v[156:159], v156 offset:38912
	ds_read_b128 v[160:163], v160 offset:45056
	ds_read_b64_tr_b16 v[164:165], v131 offset:0x2000
	ds_read_b64_tr_b16 v[166:167], v131 offset:0x2400
	ds_read_b64_tr_b16 v[168:169], v132 offset:0x2000
	ds_read_b64_tr_b16 v[170:171], v132 offset:0x2400
	ds_read_b64_tr_b16 v[172:173], v133 offset:0x2000
	ds_read_b64_tr_b16 v[174:175], v133 offset:0x2400
	ds_read_b64_tr_b16 v[176:177], v134 offset:0x2000
	ds_read_b64_tr_b16 v[178:179], v134 offset:0x2400
	s_waitcnt lgkmcnt(0)
	s_setprio 1
	s_waitcnt lgkmcnt(4)
	v_mfma_f32_16x16x32_f16 v[92:95], v[164:167], v[112:115], v[92:95]
	v_mfma_f32_16x16x32_f16 v[88:91], v[168:171], v[112:115], v[88:91]
	v_mfma_f32_16x16x32_f16 v[84:87], v[172:175], v[112:115], v[84:87]
	v_mfma_f32_16x16x32_f16 v[80:83], v[176:179], v[112:115], v[80:83]
	s_waitcnt lgkmcnt(1)
	v_mfma_f32_16x16x32_f16 v[76:79], v[164:167], v[156:159], v[76:79]
	v_mfma_f32_16x16x32_f16 v[72:75], v[168:171], v[156:159], v[72:75]
	v_mfma_f32_16x16x32_f16 v[68:71], v[172:175], v[156:159], v[68:71]
	v_mfma_f32_16x16x32_f16 v[64:67], v[176:179], v[156:159], v[64:67]
	v_mfma_f32_16x16x32_f16 v[60:63], v[164:167], v[116:119], v[60:63]
	v_mfma_f32_16x16x32_f16 v[56:59], v[168:171], v[116:119], v[56:59]
	v_mfma_f32_16x16x32_f16 v[52:55], v[172:175], v[116:119], v[52:55]
	v_mfma_f32_16x16x32_f16 v[48:51], v[176:179], v[116:119], v[48:51]
	v_mfma_f32_16x16x32_f16 v[44:47], v[164:167], v[120:123], v[44:47]
	v_mfma_f32_16x16x32_f16 v[40:43], v[168:171], v[120:123], v[40:43]
	v_mfma_f32_16x16x32_f16 v[36:39], v[172:175], v[120:123], v[36:39]
	v_mfma_f32_16x16x32_f16 v[32:35], v[176:179], v[120:123], v[32:35]
	s_waitcnt lgkmcnt(0)
	v_mfma_f32_16x16x32_f16 v[28:31], v[164:167], v[160:163], v[28:31]
	v_mfma_f32_16x16x32_f16 v[24:27], v[168:171], v[160:163], v[24:27]
	v_mfma_f32_16x16x32_f16 v[20:23], v[172:175], v[160:163], v[20:23]
	v_mfma_f32_16x16x32_f16 v[16:19], v[176:179], v[160:163], v[16:19]

.LBB2_78:
	s_mov_b64 exec, -1
.Lw2k_tail:
	s_cmp_eq_u32 s96, 0
	s_cbranch_scc1 .Lw2k_end
	global_load_dwordx4 v[208:211], v216, s[92:93] nt
	global_load_dwordx4 v[212:215], v216, s[92:93] offset:1024 nt
	s_add_u32 s92, s92, 0x400000
	s_addc_u32 s93, s93, 0
	s_sub_u32 s96, s96, 1
	s_waitcnt vmcnt(0)
	v_cvt_pk_f16_f32 v208, v208, v209
	v_cvt_pk_f16_f32 v209, v210, v211
	v_cvt_pk_f16_f32 v210, v212, v213
	v_cvt_pk_f16_f32 v211, v214, v215
	global_store_dwordx2 v217, v[208:209], s[94:95]
	global_store_dwordx2 v217, v[210:211], s[94:95] offset:512
	s_add_u32 s94, s94, 0x200000
	s_addc_u32 s95, s95, 0
	s_branch .Lw2k_tail

	.amdhsa_kernel _Z8moe_gemmILi1024ELi2048ELb1EEvPKDF16_S1_PKfPDF16_PfPKiS7_
		.amdhsa_group_segment_fixed_size 0
		.amdhsa_private_segment_fixed_size 0
		.amdhsa_kernarg_size 312
		.amdhsa_user_sgpr_count 2
		.amdhsa_user_sgpr_dispatch_ptr 0
		.amdhsa_user_sgpr_queue_ptr 0
		.amdhsa_user_sgpr_kernarg_segment_ptr 1
		.amdhsa_user_sgpr_dispatch_id 0
		.amdhsa_user_sgpr_kernarg_preload_length 0
		.amdhsa_user_sgpr_kernarg_preload_offset 0
		.amdhsa_user_sgpr_private_segment_size 0
		.amdhsa_uses_dynamic_stack 0
		.amdhsa_enable_private_segment 0
		.amdhsa_system_sgpr_workgroup_id_x 1
		.amdhsa_system_sgpr_workgroup_id_y 0
		.amdhsa_system_sgpr_workgroup_id_z 0
		.amdhsa_system_sgpr_workgroup_info 0
		.amdhsa_system_vgpr_workitem_id 0
		.amdhsa_next_free_vgpr 218
		.amdhsa_next_free_sgpr 100
		.amdhsa_accum_offset 220
		.amdhsa_reserve_vcc 1
		.amdhsa_float_round_mode_32 0
		.amdhsa_float_round_mode_16_64 0
		.amdhsa_float_denorm_mode_32 3
		.amdhsa_float_denorm_mode_16_64 3
		.amdhsa_dx10_clamp 1
		.amdhsa_ieee_mode 1
		.amdhsa_fp16_overflow 0
		.amdhsa_tg_split 0
		.amdhsa_exception_fp_ieee_invalid_op 0
		.amdhsa_exception_fp_denorm_src 0
		.amdhsa_exception_fp_ieee_div_zero 0
		.amdhsa_exception_fp_ieee_overflow 0
		.amdhsa_exception_fp_ieee_underflow 0
		.amdhsa_exception_fp_ieee_inexact 0
		.amdhsa_exception_int_div_zero 0
	.end_amdhsa_kernel

amdhsa.kernels:
  - .agpr_count:     0
    .args:
      - .actual_access:  read_only
        .address_space:  global
        .offset:         0
        .size:           8
        .value_kind:     global_buffer
      - .address_space:  global
        .offset:         8
        .size:           8
        .value_kind:     global_buffer
      - .actual_access:  read_only
        .address_space:  global
        .offset:         16
        .size:           8
        .value_kind:     global_buffer
      - .address_space:  global
        .offset:         24
        .size:           8
        .value_kind:     global_buffer
      - .offset:         32
        .size:           4
        .value_kind:     by_value
      - .actual_access:  write_only
        .address_space:  global
        .offset:         40
        .size:           8
        .value_kind:     global_buffer
      - .offset:         48
        .size:           4
        .value_kind:     hidden_block_count_x
      - .offset:         52
        .size:           4
        .value_kind:     hidden_block_count_y
      - .offset:         56
        .size:           4
        .value_kind:     hidden_block_count_z
      - .offset:         60
        .size:           2
        .value_kind:     hidden_group_size_x
      - .offset:         62
        .size:           2
        .value_kind:     hidden_group_size_y
      - .offset:         64
        .size:           2
        .value_kind:     hidden_group_size_z
      - .offset:         66
        .size:           2
        .value_kind:     hidden_remainder_x
      - .offset:         68
        .size:           2
        .value_kind:     hidden_remainder_y
      - .offset:         70
        .size:           2
        .value_kind:     hidden_remainder_z
      - .offset:         88
        .size:           8
        .value_kind:     hidden_global_offset_x
      - .offset:         96
        .size:           8
        .value_kind:     hidden_global_offset_y
      - .offset:         104
        .size:           8
        .value_kind:     hidden_global_offset_z
      - .offset:         112
        .size:           2
        .value_kind:     hidden_grid_dims
    .group_segment_fixed_size: 0
    .kernarg_segment_align: 8
    .kernarg_segment_size: 304
    .language:       OpenCL C
    .language_version:
      - 2
      - 0
    .max_flat_workgroup_size: 256
    .name:           _Z5cvt_wPKfPDF16_S0_S1_iPi
    .private_segment_fixed_size: 0
    .sgpr_count:     30
    .sgpr_spill_count: 0
    .symbol:         _Z5cvt_wPKfPDF16_S0_S1_iPi.kd
    .uniform_work_group_size: 1
    .uses_dynamic_stack: false
    .vgpr_count:     40
    .vgpr_spill_count: 0
    .wavefront_size: 64
  - .agpr_count:     0
    .args:
      - .actual_access:  read_only
        .address_space:  global
        .offset:         0
        .size:           8
        .value_kind:     global_buffer
      - .actual_access:  read_only
        .address_space:  global
        .offset:         8
        .size:           8
        .value_kind:     global_buffer
      - .actual_access:  read_only
        .address_space:  global
        .offset:         16
        .size:           8
        .value_kind:     global_buffer
      - .actual_access:  write_only
        .address_space:  global
        .offset:         24
        .size:           8
        .value_kind:     global_buffer
      - .address_space:  global
        .offset:         32
        .size:           8
        .value_kind:     global_buffer
      - .actual_access:  write_only
        .address_space:  global
        .offset:         40
        .size:           8
        .value_kind:     global_buffer
      - .actual_access:  write_only
        .address_space:  global
        .offset:         48
        .size:           8
        .value_kind:     global_buffer
      - .actual_access:  read_only
        .address_space:  global
        .offset:         56
        .size:           8
        .value_kind:     global_buffer
      - .address_space:  global
        .offset:         64
        .size:           8
        .value_kind:     global_buffer
      - .offset:         72
        .size:           4
        .value_kind:     by_value
      - .offset:         80
        .size:           4
        .value_kind:     hidden_block_count_x
      - .offset:         84
        .size:           4
        .value_kind:     hidden_block_count_y
      - .offset:         88
        .size:           4
        .value_kind:     hidden_block_count_z
      - .offset:         92
        .size:           2
        .value_kind:     hidden_group_size_x
      - .offset:         94
        .size:           2
        .value_kind:     hidden_group_size_y
      - .offset:         96
        .size:           2
        .value_kind:     hidden_group_size_z
      - .offset:         98
        .size:           2
        .value_kind:     hidden_remainder_x
      - .offset:         100
        .size:           2
        .value_kind:     hidden_remainder_y
      - .offset:         102
        .size:           2
        .value_kind:     hidden_remainder_z
      - .offset:         120
        .size:           8
        .value_kind:     hidden_global_offset_x
      - .offset:         128
        .size:           8
        .value_kind:     hidden_global_offset_y
      - .offset:         136
        .size:           8
        .value_kind:     hidden_global_offset_z
      - .offset:         144
        .size:           2
        .value_kind:     hidden_grid_dims
    .group_segment_fixed_size: 32928
    .kernarg_segment_align: 8
    .kernarg_segment_size: 336
    .language:       OpenCL C
    .language_version:
      - 2
      - 0
    .max_flat_workgroup_size: 512
    .name:           _Z11gate_kernelPKfS0_S0_PDF16_PiS2_PfS0_S1_i
    .private_segment_fixed_size: 0
    .sgpr_count:     66
    .sgpr_spill_count: 0
    .symbol:         _Z11gate_kernelPKfS0_S0_PDF16_PiS2_PfS0_S1_i.kd
    .uniform_work_group_size: 1
    .uses_dynamic_stack: false
    .vgpr_count:     115
    .vgpr_spill_count: 0
    .wavefront_size: 64
  - .agpr_count:     0
    .args:
      - .address_space:  global
        .offset:         0
        .size:           8
        .value_kind:     global_buffer
      - .address_space:  global
        .offset:         8
        .size:           8
        .value_kind:     global_buffer
      - .actual_access:  read_only
        .address_space:  global
        .offset:         16
        .size:           8
        .value_kind:     global_buffer
      - .address_space:  global
        .offset:         24
        .size:           8
        .value_kind:     global_buffer
      - .actual_access:  read_only
        .address_space:  global
        .offset:         32
        .size:           8
        .value_kind:     global_buffer
      - .actual_access:  read_only
        .address_space:  global
        .offset:         40
        .size:           8
        .value_kind:     global_buffer
      - .actual_access:  read_only
        .address_space:  global
        .offset:         48
        .size:           8
        .value_kind:     global_buffer
      - .offset:         56
        .size:           4
        .value_kind:     hidden_block_count_x
      - .offset:         60
        .size:           4
        .value_kind:     hidden_block_count_y
      - .offset:         64
        .size:           4
        .value_kind:     hidden_block_count_z
      - .offset:         68
        .size:           2
        .value_kind:     hidden_group_size_x
      - .offset:         70
        .size:           2
        .value_kind:     hidden_group_size_y
      - .offset:         72
        .size:           2
        .value_kind:     hidden_group_size_z
      - .offset:         74
        .size:           2
        .value_kind:     hidden_remainder_x
      - .offset:         76
        .size:           2
        .value_kind:     hidden_remainder_y
      - .offset:         78
        .size:           2
        .value_kind:     hidden_remainder_z
      - .offset:         96
        .size:           8
        .value_kind:     hidden_global_offset_x
      - .offset:         104
        .size:           8
        .value_kind:     hidden_global_offset_y
      - .offset:         112
        .size:           8
        .value_kind:     hidden_global_offset_z
      - .offset:         120
        .size:           2
        .value_kind:     hidden_grid_dims
      - .offset:         176
        .size:           4
        .value_kind:     hidden_dynamic_lds_size
    .group_segment_fixed_size: 0
    .kernarg_segment_align: 8
    .kernarg_segment_size: 312
    .language:       OpenCL C
    .language_version:
      - 2
      - 0
    .max_flat_workgroup_size: 256
    .name:           _Z8moe_gemmILi1024ELi2048ELb1EEvPKDF16_S1_PKfPDF16_PfPKiS7_
    .private_segment_fixed_size: 0
    .sgpr_count:     106
    .sgpr_spill_count: 0
    .symbol:         _Z8moe_gemmILi1024ELi2048ELb1EEvPKDF16_S1_PKfPDF16_PfPKiS7_.kd
    .uniform_work_group_size: 1
    .uses_dynamic_stack: false
    .vgpr_count:     218
    .vgpr_spill_count: 0
    .wavefront_size: 64
  - .agpr_count:     256
    .args:
      - .address_space:  global
        .offset:         0
        .size:           8
        .value_kind:     global_buffer
      - .address_space:  global
        .offset:         8
        .size:           8
        .value_kind:     global_buffer
      - .actual_access:  read_only
        .address_space:  global
        .offset:         16
        .size:           8
        .value_kind:     global_buffer
      - .actual_access:  read_only
        .address_space:  global
        .offset:         24
        .size:           8
        .value_kind:     global_buffer
      - .address_space:  global
        .offset:         32
        .size:           8
        .value_kind:     global_buffer
      - .actual_access:  read_only
        .address_space:  global
        .offset:         40
        .size:           8
        .value_kind:     global_buffer
      - .actual_access:  read_only
        .address_space:  global
        .offset:         48
        .size:           8
        .value_kind:     global_buffer
      - .offset:         56
        .size:           4
        .value_kind:     hidden_block_count_x
      - .offset:         60
        .size:           4
        .value_kind:     hidden_block_count_y
      - .offset:         64
        .size:           4
        .value_kind:     hidden_block_count_z
      - .offset:         68
        .size:           2
        .value_kind:     hidden_group_size_x
      - .offset:         70
        .size:           2
        .value_kind:     hidden_group_size_y
      - .offset:         72
        .size:           2
        .value_kind:     hidden_group_size_z
      - .offset:         74
        .size:           2
        .value_kind:     hidden_remainder_x
      - .offset:         76
        .size:           2
        .value_kind:     hidden_remainder_y
      - .offset:         78
        .size:           2
        .value_kind:     hidden_remainder_z
      - .offset:         96
        .size:           8
        .value_kind:     hidden_global_offset_x
      - .offset:         104
        .size:           8
        .value_kind:     hidden_global_offset_y
      - .offset:         112
        .size:           8
        .value_kind:     hidden_global_offset_z
      - .offset:         120
        .size:           2
        .value_kind:     hidden_grid_dims
      - .offset:         176
        .size:           4
        .value_kind:     hidden_dynamic_lds_size
    .group_segment_fixed_size: 86016
    .kernarg_segment_align: 8
    .kernarg_segment_size: 312
    .language:       OpenCL C
    .language_version:
      - 2
      - 0
    .max_flat_workgroup_size: 256
    .name:           _Z8moe_gemmILi2048ELi1024ELb0EEvPKDF16_S1_PKfPDF16_PfPKiS7_
    .private_segment_fixed_size: 0
    .sgpr_count:     96
    .sgpr_spill_count: 0
    .symbol:         _Z8moe_gemmILi2048ELi1024ELb0EEvPKDF16_S1_PKfPDF16_PfPKiS7_.kd
    .uniform_work_group_size: 1
    .uses_dynamic_stack: false
    .vgpr_count:     512
    .vgpr_spill_count: 0
    .wavefront_size: 64
